# attn_ret moved into MIX2, select rows balanced, gdn_scan waits counted/loads before stores, idx head loop software-pipelined
# speedup vs baseline: 1.0122x; 1.0015x over previous
.LBB0_488:
	s_mov_b64 s[28:29], -1
	s_and_b64 vcc, exec, s[24:25]
	s_waitcnt lgkmcnt(0)
	s_barrier
	s_cbranch_vccz .LBB0_492
	s_lshl_b64 s[24:25], s[26:27], 9
	s_lshl_b64 s[24:25], s[24:25], 2
	v_and_b32_e32 v18, 31, v2
	s_add_u32 s28, s6, s24
	s_addc_u32 s29, s7, s25
	s_lshl_b32 s9, s38, 2
	v_lshl_or_b32 v160, s35, 5, v18
	s_add_u32 s38, s28, s9
	v_ashrrev_i32_e32 v161, 31, v160
	v_bfe_u32 v19, v2, 5, 1
	s_addc_u32 s39, s29, 0
	v_lshlrev_b64 v[4:5], 2, v[160:161]
	v_lshl_add_u64 v[6:7], s[38:39], 0, v[4:5]
	v_lshlrev_b32_e32 v2, 13, v19
	v_lshl_add_u64 v[6:7], v[6:7], 0, v[2:3]
	s_mov_b32 s35, 0x41a00000
	v_add_co_u32_e32 v10, vcc, s35, v6
	s_mov_b64 s[38:39], 0x41a00000
	s_nop 0
	v_addc_co_u32_e32 v11, vcc, 0, v7, vcc
	v_add_co_u32_e32 v12, vcc, s43, v6
	v_lshl_add_u64 v[8:9], v[6:7], 0, s[38:39]
	s_nop 0
	v_addc_co_u32_e32 v13, vcc, 0, v7, vcc
	v_add_co_u32_e32 v14, vcc, s44, v6
	s_mov_b32 s35, 0x41a1d000
	s_nop 0
	v_addc_co_u32_e32 v15, vcc, 0, v7, vcc
	v_add_co_u32_e32 v16, vcc, s45, v6
	s_lshl_b32 s28, s8, 6
	s_nop 0
	v_addc_co_u32_e32 v17, vcc, 0, v7, vcc
	global_load_dword v166, v[10:11], off
	global_load_dword v164, v[12:13], off
	global_load_dword v165, v[12:13], off offset:2048
	global_load_dword v168, v[14:15], off
	global_load_dword v169, v[14:15], off offset:2048
	global_load_dword v170, v[16:17], off
	global_load_dword v171, v[16:17], off offset:2048
	global_load_dword v167, v[8:9], off offset:2048
	v_add_co_u32_e32 v8, vcc, s46, v6
	s_ashr_i32 s29, s28, 31
	s_nop 0
	v_addc_co_u32_e32 v9, vcc, 0, v7, vcc
	v_add_co_u32_e32 v10, vcc, s47, v6
	s_lshl_b64 s[28:29], s[28:29], 2
	s_nop 0
	v_addc_co_u32_e32 v11, vcc, 0, v7, vcc
	v_add_co_u32_e32 v12, vcc, s48, v6
	s_add_u32 s40, s6, s28
	s_nop 0
	v_addc_co_u32_e32 v13, vcc, 0, v7, vcc
	v_add_co_u32_e32 v14, vcc, s49, v6
	s_addc_u32 s41, s7, s29
	s_nop 0
	v_addc_co_u32_e32 v15, vcc, 0, v7, vcc
	global_load_dword v180, v[8:9], off
	global_load_dword v181, v[8:9], off offset:2048
	global_load_dword v194, v[10:11], off
	global_load_dword v195, v[10:11], off offset:2048
	global_load_dword v196, v[12:13], off
	global_load_dword v197, v[12:13], off offset:2048
	global_load_dword v198, v[14:15], off
	global_load_dword v199, v[14:15], off offset:2048
	v_add_co_u32_e32 v8, vcc, s50, v6
	s_add_u32 s28, s28, 0x49250004
	s_nop 0
	v_addc_co_u32_e32 v9, vcc, 0, v7, vcc
	v_add_co_u32_e32 v10, vcc, s51, v6
	s_addc_u32 s29, s29, 0
	s_nop 0
	v_addc_co_u32_e32 v11, vcc, 0, v7, vcc
	v_add_co_u32_e32 v12, vcc, s52, v6
	s_lshl_b64 s[26:27], s[26:27], 11
	s_nop 0
	v_addc_co_u32_e32 v13, vcc, 0, v7, vcc
	v_add_co_u32_e32 v14, vcc, s53, v6
	v_lshlrev_b32_e32 v149, 3, v19
	s_nop 0
	v_addc_co_u32_e32 v15, vcc, 0, v7, vcc
	global_load_dword v172, v[8:9], off
	global_load_dword v173, v[8:9], off offset:2048
	global_load_dword v174, v[10:11], off
	global_load_dword v175, v[10:11], off offset:2048
	global_load_dword v176, v[12:13], off
	global_load_dword v177, v[12:13], off offset:2048
	global_load_dword v178, v[14:15], off
	global_load_dword v179, v[14:15], off offset:2048
	v_add_co_u32_e32 v8, vcc, s54, v6
	v_mul_u32_u24_e32 v155, 0x108, v18
	s_nop 0
	v_addc_co_u32_e32 v9, vcc, 0, v7, vcc
	v_add_co_u32_e32 v10, vcc, s55, v6
	v_mul_u32_u24_e32 v153, 0x88, v18
	s_nop 0
	v_addc_co_u32_e32 v11, vcc, 0, v7, vcc
	v_add_co_u32_e32 v12, vcc, s56, v6
	v_add_u32_e32 v157, s42, v149
	s_nop 0
	v_addc_co_u32_e32 v13, vcc, 0, v7, vcc
	v_add_co_u32_e32 v6, vcc, s35, v6
	s_mov_b32 s35, 0x49250000
	s_nop 0
	v_addc_co_u32_e32 v7, vcc, 0, v7, vcc
	global_load_dword v202, v[8:9], off
	global_load_dword v203, v[8:9], off offset:2048
	global_load_dword v204, v[10:11], off
	global_load_dword v205, v[10:11], off offset:2048
	global_load_dword v206, v[12:13], off
	global_load_dword v207, v[12:13], off offset:2048
	global_load_dword v208, v[6:7], off
	global_load_dword v209, v[6:7], off offset:2048
	v_mov_b32_e32 v6, s40
	v_mov_b32_e32 v7, s41
	v_add_co_u32_e32 v6, vcc, s35, v6
	s_mov_b32 s35, 0
	s_nop 0
	v_addc_co_u32_e32 v7, vcc, 0, v7, vcc
	global_load_dword v201, v[6:7], off
	v_lshl_add_u64 v[6:7], v[2:3], 0, s[26:27]
	s_and_b32 s26, s8, 3
	v_lshl_or_b32 v6, s26, 9, v6
	v_lshl_add_u64 v[162:163], v[6:7], 0, v[4:5]
	v_mov_b32_e32 v4, 0
	v_mov_b32_e32 v5, v4
	v_mov_b32_e32 v6, v4
	v_mov_b32_e32 v7, v4
	v_mov_b32_e32 v8, v4
	v_mov_b32_e32 v9, v4
	v_mov_b32_e32 v10, v4
	v_mov_b32_e32 v11, v4
	v_mov_b32_e32 v12, v4
	v_mov_b32_e32 v13, v4
	v_mov_b32_e32 v14, v4
	v_mov_b32_e32 v15, v4
	v_mov_b32_e32 v16, v4
	v_mov_b32_e32 v17, v4
	v_mov_b32_e32 v18, v4
	v_mov_b32_e32 v19, v4
	v_mov_b32_e32 v20, v4
	v_mov_b32_e32 v21, v4
	v_mov_b32_e32 v22, v4
	v_mov_b32_e32 v23, v4
	v_mov_b32_e32 v24, v4
	v_mov_b32_e32 v25, v4
	v_mov_b32_e32 v26, v4
	v_mov_b32_e32 v27, v4
	v_mov_b32_e32 v28, v4
	v_mov_b32_e32 v29, v4
	v_mov_b32_e32 v30, v4
	v_mov_b32_e32 v31, v4
	v_mov_b32_e32 v32, v4
	v_mov_b32_e32 v33, v4
	v_mov_b32_e32 v34, v4
	v_mov_b32_e32 v35, v4
	v_mov_b32_e32 v36, v4
	v_mov_b32_e32 v37, v4
	v_mov_b32_e32 v38, v4
	v_mov_b32_e32 v39, v4
	v_mov_b32_e32 v40, v4
	v_mov_b32_e32 v41, v4
	v_mov_b32_e32 v42, v4
	v_mov_b32_e32 v43, v4
	v_mov_b32_e32 v44, v4
	v_mov_b32_e32 v45, v4
	v_mov_b32_e32 v46, v4
	v_mov_b32_e32 v47, v4
	v_mov_b32_e32 v48, v4
	v_mov_b32_e32 v49, v4
	v_mov_b32_e32 v50, v4
	v_mov_b32_e32 v51, v4
	v_mov_b32_e32 v52, v4
	v_mov_b32_e32 v53, v4
	v_mov_b32_e32 v54, v4
	v_mov_b32_e32 v55, v4
	v_mov_b32_e32 v56, v4
	v_mov_b32_e32 v57, v4
	v_mov_b32_e32 v58, v4
	v_mov_b32_e32 v59, v4
	v_mov_b32_e32 v60, v4
	v_mov_b32_e32 v61, v4
	v_mov_b32_e32 v62, v4
	v_mov_b32_e32 v63, v4
	v_mov_b32_e32 v64, v4
	v_mov_b32_e32 v65, v4
	v_mov_b32_e32 v66, v4
	v_mov_b32_e32 v67, v4
	s_mov_b64 s[38:39], 0x20000
	s_waitcnt vmcnt(0)
.LBB0_490:
	s_bitcmp1_b32 s35, 0
	s_cselect_b32 s26, 0xea00, 0
	v_add_u32_e32 v159, s26, v157
	v_add_u32_e32 v190, v159, v155
	ds_read2_b64 v[68:71], v190 offset1:2
	ds_read2_b64 v[84:87], v190 offset0:4 offset1:6
	ds_read2_b64 v[88:91], v190 offset0:8 offset1:10
	ds_read2_b64 v[92:95], v190 offset0:12 offset1:14
	ds_read2_b64 v[96:99], v190 offset0:16 offset1:18
	ds_read2_b64 v[100:103], v190 offset0:20 offset1:22
	ds_read2_b64 v[104:107], v190 offset0:24 offset1:26
	ds_read2_b64 v[108:111], v190 offset0:28 offset1:30
	v_cvt_pk_bf16_f32 v116, v52, v53
	v_cvt_pk_bf16_f32 v117, v54, v55
	v_cvt_pk_bf16_f32 v118, v56, v57
	v_cvt_pk_bf16_f32 v119, v58, v59
	v_cvt_pk_bf16_f32 v120, v60, v61
	v_cvt_pk_bf16_f32 v121, v62, v63
	v_cvt_pk_bf16_f32 v122, v64, v65
	v_cvt_pk_bf16_f32 v123, v66, v67
	v_cvt_pk_bf16_f32 v124, v36, v37
	v_cvt_pk_bf16_f32 v125, v38, v39
	v_cvt_pk_bf16_f32 v126, v40, v41
	v_cvt_pk_bf16_f32 v127, v42, v43
	v_cvt_pk_bf16_f32 v128, v44, v45
	v_cvt_pk_bf16_f32 v129, v46, v47
	v_cvt_pk_bf16_f32 v130, v48, v49
	v_cvt_pk_bf16_f32 v131, v50, v51
	v_cvt_pk_bf16_f32 v132, v20, v21
	v_cvt_pk_bf16_f32 v133, v22, v23
	v_cvt_pk_bf16_f32 v134, v24, v25
	v_cvt_pk_bf16_f32 v135, v26, v27
	v_cvt_pk_bf16_f32 v136, v28, v29
	v_cvt_pk_bf16_f32 v137, v30, v31
	v_cvt_pk_bf16_f32 v138, v32, v33
	v_cvt_pk_bf16_f32 v139, v34, v35
	v_cvt_pk_bf16_f32 v140, v4, v5
	v_cvt_pk_bf16_f32 v141, v6, v7
	v_cvt_pk_bf16_f32 v142, v8, v9
	v_cvt_pk_bf16_f32 v143, v10, v11
	v_cvt_pk_bf16_f32 v144, v12, v13
	v_cvt_pk_bf16_f32 v145, v14, v15
	v_cvt_pk_bf16_f32 v146, v16, v17
	v_cvt_pk_bf16_f32 v147, v18, v19
	s_waitcnt lgkmcnt(0)
	v_mfma_f32_32x32x16_bf16 v[68:83], v[68:71], v[116:119], 0
	v_mfma_f32_32x32x16_bf16 v[68:83], v[84:87], v[120:123], v[68:83]
	v_mfma_f32_32x32x16_bf16 v[68:83], v[88:91], v[124:127], v[68:83]
	v_mfma_f32_32x32x16_bf16 v[68:83], v[92:95], v[128:131], v[68:83]
	v_mfma_f32_32x32x16_bf16 v[68:83], v[96:99], v[132:135], v[68:83]
	v_mfma_f32_32x32x16_bf16 v[68:83], v[100:103], v[136:139], v[68:83]
	v_mfma_f32_32x32x16_bf16 v[68:83], v[104:107], v[140:143], v[68:83]
	v_mfma_f32_32x32x16_bf16 v[68:83], v[108:111], v[144:147], v[68:83]
	v_add_u32_e32 v88, 0x2000, v190
	ds_read2_b64 v[84:87], v88 offset0:32 offset1:34
	ds_read2_b64 v[100:103], v88 offset0:36 offset1:38
	ds_read2_b64 v[104:107], v88 offset0:40 offset1:42
	ds_read2_b64 v[108:111], v88 offset0:44 offset1:46
	ds_read2_b64 v[112:115], v88 offset0:48 offset1:50
	ds_read2_b64 v[182:185], v88 offset0:52 offset1:54
	ds_read2_b64 v[186:189], v88 offset0:56 offset1:58
	ds_read2_b64 v[214:217], v88 offset0:60 offset1:62
	s_waitcnt lgkmcnt(0)
	v_mfma_f32_32x32x16_bf16 v[84:99], v[84:87], v[116:119], 0
	v_mfma_f32_32x32x16_bf16 v[84:99], v[100:103], v[120:123], v[84:99]
	v_mfma_f32_32x32x16_bf16 v[84:99], v[104:107], v[124:127], v[84:99]
	v_mfma_f32_32x32x16_bf16 v[84:99], v[108:111], v[128:131], v[84:99]
	v_mfma_f32_32x32x16_bf16 v[84:99], v[112:115], v[132:135], v[84:99]
	v_mfma_f32_32x32x16_bf16 v[84:99], v[182:185], v[136:139], v[84:99]
	v_mfma_f32_32x32x16_bf16 v[84:99], v[186:189], v[140:143], v[84:99]
	v_mfma_f32_32x32x16_bf16 v[84:99], v[214:217], v[144:147], v[84:99]
	s_waitcnt vmcnt(32)
	v_mov_b32_e32 v200, v201
	v_sub_f32_e32 v81, v197, v81
	v_sub_f32_e32 v80, v196, v80
	v_sub_f32_e32 v71, v165, v71
	v_sub_f32_e32 v70, v164, v70
	v_sub_f32_e32 v69, v167, v69
	v_sub_f32_e32 v68, v166, v68
	v_cvt_pk_bf16_f32 v106, v80, v81
	s_nop 3
	v_sub_f32_e32 v80, v175, v87
	v_sub_f32_e32 v81, v174, v86
	v_sub_f32_e32 v83, v199, v83
	v_sub_f32_e32 v82, v198, v82
	v_sub_f32_e32 v79, v195, v79
	v_sub_f32_e32 v78, v194, v78
	v_sub_f32_e32 v77, v181, v77
	v_sub_f32_e32 v76, v180, v76
	v_sub_f32_e32 v75, v171, v75
	v_sub_f32_e32 v74, v170, v74
	v_sub_f32_e32 v73, v169, v73
	v_sub_f32_e32 v72, v168, v72
	v_cvt_pk_bf16_f32 v100, v68, v69
	v_cvt_pk_bf16_f32 v101, v70, v71
	v_sub_f32_e32 v68, v179, v91
	v_sub_f32_e32 v69, v178, v90
	v_sub_f32_e32 v70, v177, v89
	v_sub_f32_e32 v71, v176, v88
	v_cvt_pk_bf16_f32 v109, v81, v80
	v_add_u32_e32 v80, 0x4000, v190
	v_cvt_pk_bf16_f32 v102, v72, v73
	v_cvt_pk_bf16_f32 v103, v74, v75
	v_cvt_pk_bf16_f32 v104, v76, v77
	v_cvt_pk_bf16_f32 v105, v78, v79
	v_cvt_pk_bf16_f32 v107, v82, v83
	v_sub_f32_e32 v72, v209, v99
	v_sub_f32_e32 v73, v208, v98
	v_sub_f32_e32 v74, v207, v97
	v_sub_f32_e32 v75, v206, v96
	v_sub_f32_e32 v76, v205, v95
	v_sub_f32_e32 v77, v204, v94
	v_sub_f32_e32 v78, v203, v93
	v_sub_f32_e32 v79, v202, v92
	v_sub_f32_e32 v82, v173, v85
	v_sub_f32_e32 v83, v172, v84
	v_cvt_pk_bf16_f32 v110, v71, v70
	v_cvt_pk_bf16_f32 v111, v69, v68
	ds_read2_b64 v[68:71], v80 offset0:64 offset1:66
	ds_read2_b64 v[84:87], v80 offset0:68 offset1:70
	ds_read2_b64 v[88:91], v80 offset0:72 offset1:74
	ds_read2_b64 v[92:95], v80 offset0:76 offset1:78
	ds_read2_b64 v[96:99], v80 offset0:80 offset1:82
	ds_read2_b64 v[164:167], v80 offset0:84 offset1:86
	ds_read2_b64 v[168:171], v80 offset0:88 offset1:90
	ds_read2_b64 v[172:175], v80 offset0:92 offset1:94
	v_cvt_pk_bf16_f32 v108, v83, v82
	v_cvt_pk_bf16_f32 v112, v79, v78
	v_cvt_pk_bf16_f32 v113, v77, v76
	v_cvt_pk_bf16_f32 v114, v75, v74
	v_cvt_pk_bf16_f32 v115, v73, v72
	s_waitcnt lgkmcnt(7)
	v_mfma_f32_32x32x16_bf16 v[68:83], v[68:71], v[116:119], 0
	s_waitcnt lgkmcnt(6)
	v_mfma_f32_32x32x16_bf16 v[68:83], v[84:87], v[120:123], v[68:83]
	s_waitcnt lgkmcnt(5)
	v_mfma_f32_32x32x16_bf16 v[68:83], v[88:91], v[124:127], v[68:83]
	s_waitcnt lgkmcnt(4)
	v_mfma_f32_32x32x16_bf16 v[68:83], v[92:95], v[128:131], v[68:83]
	s_waitcnt lgkmcnt(3)
	v_mfma_f32_32x32x16_bf16 v[68:83], v[96:99], v[132:135], v[68:83]
	s_waitcnt lgkmcnt(2)
	v_mfma_f32_32x32x16_bf16 v[68:83], v[164:167], v[136:139], v[68:83]
	s_waitcnt lgkmcnt(1)
	v_mfma_f32_32x32x16_bf16 v[68:83], v[168:171], v[140:143], v[68:83]
	s_waitcnt lgkmcnt(0)
	v_mfma_f32_32x32x16_bf16 v[68:83], v[172:175], v[144:147], v[68:83]
	v_add_u32_e32 v88, 0x6000, v190
	ds_read2_b64 v[84:87], v88 offset0:96 offset1:98
	ds_read2_b64 v[164:167], v88 offset0:100 offset1:102
	ds_read2_b64 v[168:171], v88 offset0:104 offset1:106
	ds_read2_b64 v[172:175], v88 offset0:108 offset1:110
	ds_read2_b64 v[176:179], v88 offset0:112 offset1:114
	ds_read2_b64 v[180:183], v88 offset0:116 offset1:118
	ds_read2_b64 v[184:187], v88 offset0:120 offset1:122
	ds_read2_b64 v[194:197], v88 offset0:124 offset1:126
	s_waitcnt lgkmcnt(7)
	v_mfma_f32_32x32x16_bf16 v[84:99], v[84:87], v[116:119], 0
	s_waitcnt lgkmcnt(6)
	v_mfma_f32_32x32x16_bf16 v[84:99], v[164:167], v[120:123], v[84:99]
	s_waitcnt lgkmcnt(5)
	v_mfma_f32_32x32x16_bf16 v[84:99], v[168:171], v[124:127], v[84:99]
	s_waitcnt lgkmcnt(4)
	v_mfma_f32_32x32x16_bf16 v[84:99], v[172:175], v[128:131], v[84:99]
	s_waitcnt lgkmcnt(3)
	v_mfma_f32_32x32x16_bf16 v[84:99], v[176:179], v[132:135], v[84:99]
	s_waitcnt lgkmcnt(2)
	v_mfma_f32_32x32x16_bf16 v[84:99], v[180:183], v[136:139], v[84:99]
	s_waitcnt lgkmcnt(1)
	v_mfma_f32_32x32x16_bf16 v[84:99], v[184:187], v[140:143], v[84:99]
	s_waitcnt lgkmcnt(0)
	v_mfma_f32_32x32x16_bf16 v[84:99], v[194:197], v[144:147], v[84:99]
	v_add_u32_e32 v159, v159, v153
	v_add_u32_e32 v128, 0x8000, v159
	v_add_u32_e32 v144, 0x9000, v159
	ds_read2_b64 v[116:119], v128 offset0:128 offset1:130
	ds_read2_b64 v[120:123], v128 offset0:132 offset1:134
	ds_read2_b64 v[124:127], v128 offset0:136 offset1:138
	ds_read2_b64 v[128:131], v128 offset0:140 offset1:142
	ds_read2_b64 v[132:135], v144 offset0:160 offset1:162
	ds_read2_b64 v[136:139], v144 offset0:164 offset1:166
	ds_read2_b64 v[140:143], v144 offset0:168 offset1:170
	ds_read2_b64 v[144:147], v144 offset0:172 offset1:174
	s_waitcnt lgkmcnt(7)
	v_mfma_f32_32x32x16_bf16 v[68:83], v[116:119], v[100:103], v[68:83]
	s_waitcnt lgkmcnt(3)
	v_mfma_f32_32x32x16_bf16 v[84:99], v[132:135], v[100:103], v[84:99]
	v_mfma_f32_32x32x16_bf16 v[68:83], v[120:123], v[104:107], v[68:83]
	s_waitcnt lgkmcnt(2)
	v_mfma_f32_32x32x16_bf16 v[84:99], v[136:139], v[104:107], v[84:99]
	v_mfma_f32_32x32x16_bf16 v[68:83], v[124:127], v[108:111], v[68:83]
	s_waitcnt lgkmcnt(1)
	v_mfma_f32_32x32x16_bf16 v[84:99], v[140:143], v[108:111], v[84:99]
	v_mfma_f32_32x32x16_bf16 v[68:83], v[128:131], v[112:115], v[68:83]
	s_waitcnt lgkmcnt(0)
	v_mfma_f32_32x32x16_bf16 v[84:99], v[144:147], v[112:115], v[84:99]
	v_lshl_add_u64 v[116:117], s[6:7], 0, v[162:163]
	s_mov_b32 s26, 0x41a20000
	v_add_co_u32_e32 v218, vcc, s26, v116
	s_nop 1
	v_addc_co_u32_e32 v219, vcc, 0, v117, vcc
	s_mov_b32 s26, 0x41a21000
	v_add_co_u32_e32 v220, vcc, s26, v116
	s_nop 1
	v_addc_co_u32_e32 v221, vcc, 0, v117, vcc
	s_mov_b32 s26, 0x41a24000
	v_add_co_u32_e32 v222, vcc, s26, v116
	s_nop 1
	v_addc_co_u32_e32 v223, vcc, 0, v117, vcc
	s_mov_b32 s26, 0x41a25000
	v_add_co_u32_e32 v224, vcc, s26, v116
	s_nop 1
	v_addc_co_u32_e32 v225, vcc, 0, v117, vcc
	global_load_dword v166, v[218:219], off
	global_load_dword v167, v[218:219], off offset:2048
	global_load_dword v164, v[220:221], off
	global_load_dword v165, v[220:221], off offset:2048
	global_load_dword v168, v[222:223], off
	global_load_dword v169, v[222:223], off offset:2048
	global_load_dword v170, v[224:225], off
	global_load_dword v171, v[224:225], off offset:2048
	s_mov_b32 s26, 0x41a28000
	v_add_co_u32_e32 v218, vcc, s26, v116
	s_nop 1
	v_addc_co_u32_e32 v219, vcc, 0, v117, vcc
	s_mov_b32 s26, 0x41a29000
	v_add_co_u32_e32 v220, vcc, s26, v116
	s_nop 1
	v_addc_co_u32_e32 v221, vcc, 0, v117, vcc
	s_mov_b32 s26, 0x41a2c000
	v_add_co_u32_e32 v222, vcc, s26, v116
	s_nop 1
	v_addc_co_u32_e32 v223, vcc, 0, v117, vcc
	s_mov_b32 s26, 0x41a2d000
	v_add_co_u32_e32 v224, vcc, s26, v116
	s_nop 1
	v_addc_co_u32_e32 v225, vcc, 0, v117, vcc
	global_load_dword v180, v[218:219], off
	global_load_dword v181, v[218:219], off offset:2048
	global_load_dword v194, v[220:221], off
	global_load_dword v195, v[220:221], off offset:2048
	global_load_dword v196, v[222:223], off
	global_load_dword v197, v[222:223], off offset:2048
	global_load_dword v198, v[224:225], off
	global_load_dword v199, v[224:225], off offset:2048
	s_mov_b32 s26, 0x41a30000
	v_add_co_u32_e32 v218, vcc, s26, v116
	s_nop 1
	v_addc_co_u32_e32 v219, vcc, 0, v117, vcc
	s_mov_b32 s26, 0x41a31000
	v_add_co_u32_e32 v220, vcc, s26, v116
	s_nop 1
	v_addc_co_u32_e32 v221, vcc, 0, v117, vcc
	s_mov_b32 s26, 0x41a34000
	v_add_co_u32_e32 v222, vcc, s26, v116
	s_nop 1
	v_addc_co_u32_e32 v223, vcc, 0, v117, vcc
	s_mov_b32 s26, 0x41a35000
	v_add_co_u32_e32 v224, vcc, s26, v116
	s_nop 1
	v_addc_co_u32_e32 v225, vcc, 0, v117, vcc
	global_load_dword v172, v[218:219], off
	global_load_dword v173, v[218:219], off offset:2048
	global_load_dword v174, v[220:221], off
	global_load_dword v175, v[220:221], off offset:2048
	global_load_dword v176, v[222:223], off
	global_load_dword v177, v[222:223], off offset:2048
	global_load_dword v178, v[224:225], off
	global_load_dword v179, v[224:225], off offset:2048
	s_mov_b32 s26, 0x41a38000
	v_add_co_u32_e32 v218, vcc, s26, v116
	s_nop 1
	v_addc_co_u32_e32 v219, vcc, 0, v117, vcc
	s_mov_b32 s26, 0x41a39000
	v_add_co_u32_e32 v220, vcc, s26, v116
	s_nop 1
	v_addc_co_u32_e32 v221, vcc, 0, v117, vcc
	s_mov_b32 s26, 0x41a3c000
	v_add_co_u32_e32 v222, vcc, s26, v116
	s_nop 1
	v_addc_co_u32_e32 v223, vcc, 0, v117, vcc
	s_mov_b32 s26, 0x41a3d000
	v_add_co_u32_e32 v224, vcc, s26, v116
	s_nop 1
	v_addc_co_u32_e32 v225, vcc, 0, v117, vcc
	global_load_dword v202, v[218:219], off
	global_load_dword v203, v[218:219], off offset:2048
	global_load_dword v204, v[220:221], off
	global_load_dword v205, v[220:221], off offset:2048
	global_load_dword v206, v[222:223], off
	global_load_dword v207, v[222:223], off offset:2048
	global_load_dword v208, v[224:225], off
	global_load_dword v209, v[224:225], off offset:2048
	s_add_i32 s35, s35, 1
	s_add_u32 s26, s6, s28
	s_addc_u32 s27, s7, s29
	v_mov_b64_e32 v[232:233], s[26:27]
	global_load_dword v201, v[232:233], off
	s_mov_b32 s26, 0x47200000
	v_add_co_u32_e32 v218, vcc, s26, v116
	s_nop 1
	v_addc_co_u32_e32 v219, vcc, 0, v117, vcc
	s_mov_b32 s26, 0x47201000
	v_add_co_u32_e32 v220, vcc, s26, v116
	s_nop 1
	v_addc_co_u32_e32 v221, vcc, 0, v117, vcc
	s_mov_b32 s26, 0x47204000
	v_add_co_u32_e32 v222, vcc, s26, v116
	s_nop 1
	v_addc_co_u32_e32 v223, vcc, 0, v117, vcc
	s_mov_b32 s26, 0x47205000
	v_add_co_u32_e32 v224, vcc, s26, v116
	s_nop 1
	v_addc_co_u32_e32 v225, vcc, 0, v117, vcc
	global_store_dword v[218:219], v68, off
	global_store_dword v[218:219], v69, off offset:2048
	global_store_dword v[220:221], v70, off
	global_store_dword v[220:221], v71, off offset:2048
	global_store_dword v[222:223], v72, off
	global_store_dword v[222:223], v73, off offset:2048
	global_store_dword v[224:225], v74, off
	global_store_dword v[224:225], v75, off offset:2048
	s_mov_b32 s26, 0x47208000
	v_add_co_u32_e32 v218, vcc, s26, v116
	s_nop 1
	v_addc_co_u32_e32 v219, vcc, 0, v117, vcc
	s_mov_b32 s26, 0x47209000
	v_add_co_u32_e32 v220, vcc, s26, v116
	s_nop 1
	v_addc_co_u32_e32 v221, vcc, 0, v117, vcc
	s_mov_b32 s26, 0x4720c000
	v_add_co_u32_e32 v222, vcc, s26, v116
	s_nop 1
	v_addc_co_u32_e32 v223, vcc, 0, v117, vcc
	s_mov_b32 s26, 0x4720d000
	v_add_co_u32_e32 v224, vcc, s26, v116
	s_nop 1
	v_addc_co_u32_e32 v225, vcc, 0, v117, vcc
	global_store_dword v[218:219], v76, off
	global_store_dword v[218:219], v77, off offset:2048
	global_store_dword v[220:221], v78, off
	global_store_dword v[220:221], v79, off offset:2048
	global_store_dword v[222:223], v80, off
	global_store_dword v[222:223], v81, off offset:2048
	global_store_dword v[224:225], v82, off
	global_store_dword v[224:225], v83, off offset:2048
	s_mov_b32 s26, 0x47210000
	v_add_co_u32_e32 v218, vcc, s26, v116
	s_nop 1
	v_addc_co_u32_e32 v219, vcc, 0, v117, vcc
	s_mov_b32 s26, 0x47211000
	v_add_co_u32_e32 v220, vcc, s26, v116
	s_nop 1
	v_addc_co_u32_e32 v221, vcc, 0, v117, vcc
	s_mov_b32 s26, 0x47214000
	v_add_co_u32_e32 v222, vcc, s26, v116
	s_nop 1
	v_addc_co_u32_e32 v223, vcc, 0, v117, vcc
	s_mov_b32 s26, 0x47215000
	v_add_co_u32_e32 v224, vcc, s26, v116
	s_nop 1
	v_addc_co_u32_e32 v225, vcc, 0, v117, vcc
	global_store_dword v[218:219], v84, off
	global_store_dword v[218:219], v85, off offset:2048
	global_store_dword v[220:221], v86, off
	global_store_dword v[220:221], v87, off offset:2048
	global_store_dword v[222:223], v88, off
	global_store_dword v[222:223], v89, off offset:2048
	global_store_dword v[224:225], v90, off
	global_store_dword v[224:225], v91, off offset:2048
	s_mov_b32 s26, 0x47218000
	v_add_co_u32_e32 v218, vcc, s26, v116
	s_nop 1
	v_addc_co_u32_e32 v219, vcc, 0, v117, vcc
	s_mov_b32 s26, 0x47219000
	v_add_co_u32_e32 v220, vcc, s26, v116
	s_nop 1
	v_addc_co_u32_e32 v221, vcc, 0, v117, vcc
	s_mov_b32 s26, 0x4721c000
	v_add_co_u32_e32 v222, vcc, s26, v116
	s_nop 1
	v_addc_co_u32_e32 v223, vcc, 0, v117, vcc
	s_mov_b32 s26, 0x4721d000
	v_add_co_u32_e32 v224, vcc, s26, v116
	s_nop 1
	v_addc_co_u32_e32 v225, vcc, 0, v117, vcc
	global_store_dword v[218:219], v92, off
	global_store_dword v[218:219], v93, off offset:2048
	global_store_dword v[220:221], v94, off
	global_store_dword v[220:221], v95, off offset:2048
	global_store_dword v[222:223], v96, off
	global_store_dword v[222:223], v97, off offset:2048
	global_store_dword v[224:225], v98, off
	global_store_dword v[224:225], v99, off offset:2048
	v_add_u32_e32 v80, 0xa000, v159
	v_add_u32_e32 v96, 0xb000, v159
	ds_read2_b64 v[68:71], v80 offset0:192 offset1:194
	ds_read2_b64 v[72:75], v80 offset0:196 offset1:198
	ds_read2_b64 v[76:79], v80 offset0:200 offset1:202
	ds_read2_b64 v[80:83], v80 offset0:204 offset1:206
	ds_read2_b64 v[84:87], v96 offset0:224 offset1:226
	ds_read2_b64 v[88:91], v96 offset0:228 offset1:230
	ds_read2_b64 v[92:95], v96 offset0:232 offset1:234
	ds_read2_b64 v[96:99], v96 offset0:236 offset1:238
	v_pk_mul_f32 v[66:67], v[66:67], v[200:201] op_sel_hi:[1,0]
	v_pk_mul_f32 v[64:65], v[64:65], v[200:201] op_sel_hi:[1,0]
	v_pk_mul_f32 v[62:63], v[62:63], v[200:201] op_sel_hi:[1,0]
	v_pk_mul_f32 v[60:61], v[60:61], v[200:201] op_sel_hi:[1,0]
	v_pk_mul_f32 v[58:59], v[58:59], v[200:201] op_sel_hi:[1,0]
	v_pk_mul_f32 v[56:57], v[56:57], v[200:201] op_sel_hi:[1,0]
	v_pk_mul_f32 v[54:55], v[54:55], v[200:201] op_sel_hi:[1,0]
	v_pk_mul_f32 v[52:53], v[52:53], v[200:201] op_sel_hi:[1,0]
	v_pk_mul_f32 v[50:51], v[50:51], v[200:201] op_sel_hi:[1,0]
	v_pk_mul_f32 v[48:49], v[48:49], v[200:201] op_sel_hi:[1,0]
	v_pk_mul_f32 v[46:47], v[46:47], v[200:201] op_sel_hi:[1,0]
	v_pk_mul_f32 v[44:45], v[44:45], v[200:201] op_sel_hi:[1,0]
	v_pk_mul_f32 v[42:43], v[42:43], v[200:201] op_sel_hi:[1,0]
	v_pk_mul_f32 v[40:41], v[40:41], v[200:201] op_sel_hi:[1,0]
	v_pk_mul_f32 v[38:39], v[38:39], v[200:201] op_sel_hi:[1,0]
	v_pk_mul_f32 v[36:37], v[36:37], v[200:201] op_sel_hi:[1,0]
	s_waitcnt lgkmcnt(0)
	v_mfma_f32_32x32x16_bf16 v[52:67], v[68:71], v[100:103], v[52:67]
	v_mfma_f32_32x32x16_bf16 v[36:51], v[84:87], v[100:103], v[36:51]
	v_mfma_f32_32x32x16_bf16 v[52:67], v[72:75], v[104:107], v[52:67]
	v_mfma_f32_32x32x16_bf16 v[36:51], v[88:91], v[104:107], v[36:51]
	v_mfma_f32_32x32x16_bf16 v[52:67], v[76:79], v[108:111], v[52:67]
	v_mfma_f32_32x32x16_bf16 v[36:51], v[92:95], v[108:111], v[36:51]
	v_mfma_f32_32x32x16_bf16 v[52:67], v[80:83], v[112:115], v[52:67]
	v_mfma_f32_32x32x16_bf16 v[36:51], v[96:99], v[112:115], v[36:51]
	v_add_u32_e32 v80, 0xc800, v159
	v_add_u32_e32 v96, 0xd800, v159
	ds_read2_b64 v[68:71], v80 offset1:2
	ds_read2_b64 v[72:75], v80 offset0:4 offset1:6
	ds_read2_b64 v[76:79], v80 offset0:8 offset1:10
	ds_read2_b64 v[80:83], v80 offset0:12 offset1:14
	ds_read2_b64 v[84:87], v96 offset0:32 offset1:34
	ds_read2_b64 v[88:91], v96 offset0:36 offset1:38
	ds_read2_b64 v[92:95], v96 offset0:40 offset1:42
	ds_read2_b64 v[96:99], v96 offset0:44 offset1:46
	v_pk_mul_f32 v[34:35], v[34:35], v[200:201] op_sel_hi:[1,0]
	v_pk_mul_f32 v[32:33], v[32:33], v[200:201] op_sel_hi:[1,0]
	v_pk_mul_f32 v[30:31], v[30:31], v[200:201] op_sel_hi:[1,0]
	v_pk_mul_f32 v[28:29], v[28:29], v[200:201] op_sel_hi:[1,0]
	v_pk_mul_f32 v[26:27], v[26:27], v[200:201] op_sel_hi:[1,0]
	v_pk_mul_f32 v[24:25], v[24:25], v[200:201] op_sel_hi:[1,0]
	v_pk_mul_f32 v[22:23], v[22:23], v[200:201] op_sel_hi:[1,0]
	v_pk_mul_f32 v[20:21], v[20:21], v[200:201] op_sel_hi:[1,0]
	v_pk_mul_f32 v[18:19], v[18:19], v[200:201] op_sel_hi:[1,0]
	v_pk_mul_f32 v[16:17], v[16:17], v[200:201] op_sel_hi:[1,0]
	v_pk_mul_f32 v[14:15], v[14:15], v[200:201] op_sel_hi:[1,0]
	v_pk_mul_f32 v[12:13], v[12:13], v[200:201] op_sel_hi:[1,0]
	v_pk_mul_f32 v[10:11], v[10:11], v[200:201] op_sel_hi:[1,0]
	v_pk_mul_f32 v[8:9], v[8:9], v[200:201] op_sel_hi:[1,0]
	v_pk_mul_f32 v[6:7], v[6:7], v[200:201] op_sel_hi:[1,0]
	v_pk_mul_f32 v[4:5], v[4:5], v[200:201] op_sel_hi:[1,0]
	s_waitcnt lgkmcnt(0)
	v_mfma_f32_32x32x16_bf16 v[20:35], v[68:71], v[100:103], v[20:35]
	v_mfma_f32_32x32x16_bf16 v[4:19], v[84:87], v[100:103], v[4:19]
	v_mfma_f32_32x32x16_bf16 v[20:35], v[72:75], v[104:107], v[20:35]
	v_mfma_f32_32x32x16_bf16 v[4:19], v[88:91], v[104:107], v[4:19]
	v_mfma_f32_32x32x16_bf16 v[20:35], v[76:79], v[108:111], v[20:35]
	v_mfma_f32_32x32x16_bf16 v[4:19], v[92:95], v[108:111], v[4:19]
	v_mfma_f32_32x32x16_bf16 v[20:35], v[80:83], v[112:115], v[20:35]
	v_mfma_f32_32x32x16_bf16 v[4:19], v[96:99], v[112:115], v[4:19]
	s_add_u32 s28, s28, 4
	s_addc_u32 s29, s29, 0
	v_lshl_add_u64 v[162:163], v[162:163], 0, s[38:39]
	s_cmp_eq_u32 s35, 63
	s_barrier
	s_cbranch_scc0 .LBB0_490
	s_waitcnt vmcnt(32)
	v_add_u32_e32 v82, v157, v155
	v_cvt_pk_bf16_f32 v52, v52, v53
	v_cvt_pk_bf16_f32 v53, v54, v55
	v_cvt_pk_bf16_f32 v54, v56, v57
	v_cvt_pk_bf16_f32 v57, v62, v63
	v_cvt_pk_bf16_f32 v62, v8, v9
	v_add_u32_e32 v8, 0xe800, v82
	v_cvt_pk_bf16_f32 v56, v60, v61
	v_cvt_pk_bf16_f32 v36, v36, v37
	v_cvt_pk_bf16_f32 v37, v38, v39
	v_cvt_pk_bf16_f32 v38, v40, v41
	v_cvt_pk_bf16_f32 v39, v42, v43
	v_cvt_pk_bf16_f32 v40, v44, v45
	v_cvt_pk_bf16_f32 v41, v46, v47
	v_cvt_pk_bf16_f32 v42, v48, v49
	v_cvt_pk_bf16_f32 v43, v50, v51
	v_cvt_pk_bf16_f32 v44, v20, v21
	v_cvt_pk_bf16_f32 v45, v22, v23
	v_cvt_pk_bf16_f32 v46, v24, v25
	v_cvt_pk_bf16_f32 v47, v26, v27
	v_cvt_pk_bf16_f32 v48, v28, v29
	v_cvt_pk_bf16_f32 v49, v30, v31
	v_cvt_pk_bf16_f32 v50, v32, v33
	v_cvt_pk_bf16_f32 v51, v34, v35
	v_cvt_pk_bf16_f32 v60, v4, v5
	v_cvt_pk_bf16_f32 v61, v6, v7
	ds_read2_b64 v[4:7], v8 offset0:64 offset1:66
	ds_read2_b64 v[20:23], v8 offset0:68 offset1:70
	ds_read2_b64 v[24:27], v8 offset0:72 offset1:74
	ds_read2_b64 v[28:31], v8 offset0:76 offset1:78
	ds_read2_b64 v[32:35], v8 offset0:80 offset1:82
	ds_read2_b64 v[68:71], v8 offset0:84 offset1:86
	ds_read2_b64 v[72:75], v8 offset0:88 offset1:90
	ds_read2_b64 v[78:81], v8 offset0:92 offset1:94
	s_add_u32 s24, s6, s24
	s_addc_u32 s25, s7, s25
	s_add_u32 s24, s24, s9
	s_addc_u32 s25, s25, 0
	v_lshl_add_u64 v[76:77], v[160:161], 2, s[24:25]
	v_cvt_pk_bf16_f32 v55, v58, v59
	v_cvt_pk_bf16_f32 v58, v64, v65
	v_cvt_pk_bf16_f32 v59, v66, v67
	v_cvt_pk_bf16_f32 v63, v10, v11
	v_cvt_pk_bf16_f32 v64, v12, v13
	v_cvt_pk_bf16_f32 v65, v14, v15
	v_cvt_pk_bf16_f32 v66, v16, v17
	v_cvt_pk_bf16_f32 v67, v18, v19
	s_waitcnt lgkmcnt(7)
	v_mfma_f32_32x32x16_bf16 v[4:19], v[4:7], v[52:55], 0
	s_waitcnt lgkmcnt(6)
	v_mfma_f32_32x32x16_bf16 v[4:19], v[20:23], v[56:59], v[4:19]
	s_waitcnt lgkmcnt(5)
	v_mfma_f32_32x32x16_bf16 v[4:19], v[24:27], v[36:39], v[4:19]
	s_waitcnt lgkmcnt(4)
	v_mfma_f32_32x32x16_bf16 v[4:19], v[28:31], v[40:43], v[4:19]
	s_waitcnt lgkmcnt(3)
	v_mfma_f32_32x32x16_bf16 v[4:19], v[32:35], v[44:47], v[4:19]
	s_waitcnt lgkmcnt(2)
	v_mfma_f32_32x32x16_bf16 v[4:19], v[68:71], v[48:51], v[4:19]
	s_waitcnt lgkmcnt(1)
	v_mfma_f32_32x32x16_bf16 v[4:19], v[72:75], v[60:63], v[4:19]
	s_waitcnt lgkmcnt(0)
	v_mfma_f32_32x32x16_bf16 v[4:19], v[78:81], v[64:67], v[4:19]
	v_add_u32_e32 v20, 0x2100, v82
	v_add_u32_e32 v24, 0xe800, v20
	ds_read2_b64 v[20:23], v24 offset0:64 offset1:66
	ds_read2_b64 v[68:71], v24 offset0:68 offset1:70
	ds_read2_b64 v[72:75], v24 offset0:72 offset1:74
	ds_read2_b64 v[78:81], v24 offset0:76 offset1:78
	ds_read2_b64 v[82:85], v24 offset0:80 offset1:82
	ds_read2_b64 v[86:89], v24 offset0:84 offset1:86
	ds_read2_b64 v[90:93], v24 offset0:88 offset1:90
	ds_read2_b64 v[94:97], v24 offset0:92 offset1:94
	s_waitcnt lgkmcnt(7)
	v_mfma_f32_32x32x16_bf16 v[20:35], v[20:23], v[52:55], 0
	s_waitcnt lgkmcnt(6)
	v_mfma_f32_32x32x16_bf16 v[20:35], v[68:71], v[56:59], v[20:35]
	s_waitcnt lgkmcnt(5)
	v_mfma_f32_32x32x16_bf16 v[20:35], v[72:75], v[36:39], v[20:35]
	s_waitcnt lgkmcnt(4)
	v_mfma_f32_32x32x16_bf16 v[20:35], v[78:81], v[40:43], v[20:35]
	s_waitcnt lgkmcnt(3)
	v_mfma_f32_32x32x16_bf16 v[20:35], v[82:85], v[44:47], v[20:35]
	s_waitcnt lgkmcnt(2)
	v_mfma_f32_32x32x16_bf16 v[20:35], v[86:89], v[48:51], v[20:35]
	s_waitcnt lgkmcnt(1)
	v_mfma_f32_32x32x16_bf16 v[20:35], v[90:93], v[60:63], v[20:35]
	s_waitcnt lgkmcnt(0)
	v_mfma_f32_32x32x16_bf16 v[20:35], v[94:97], v[64:67], v[20:35]
	v_add_f32_e64 v4, v166, -v4
	v_add_f32_e64 v5, v167, -v5
	v_add_f32_e64 v6, v164, -v6
	v_add_f32_e64 v7, v165, -v7
	v_add_f32_e64 v8, v168, -v8
	v_add_f32_e64 v9, v169, -v9
	v_pk_add_f32 v[10:11], v[170:171], v[10:11] neg_lo:[0,1] neg_hi:[0,1]
	v_pk_add_f32 v[12:13], v[180:181], v[12:13] neg_lo:[0,1] neg_hi:[0,1]
	v_pk_add_f32 v[14:15], v[194:195], v[14:15] neg_lo:[0,1] neg_hi:[0,1]
	v_pk_add_f32 v[16:17], v[196:197], v[16:17] neg_lo:[0,1] neg_hi:[0,1]
	v_pk_add_f32 v[18:19], v[198:199], v[18:19] neg_lo:[0,1] neg_hi:[0,1]
	v_cvt_pk_bf16_f32 v68, v4, v5
	v_cvt_pk_bf16_f32 v69, v6, v7
	v_pk_add_f32 v[4:5], v[172:173], v[20:21] neg_lo:[0,1] neg_hi:[0,1]
	v_pk_add_f32 v[6:7], v[174:175], v[22:23] neg_lo:[0,1] neg_hi:[0,1]
	v_add3_u32 v98, s31, v149, v155
	v_cvt_pk_bf16_f32 v70, v8, v9
	v_cvt_pk_bf16_f32 v71, v10, v11
	v_cvt_pk_bf16_f32 v72, v12, v13
	v_cvt_pk_bf16_f32 v73, v14, v15
	v_cvt_pk_bf16_f32 v74, v16, v17
	v_cvt_pk_bf16_f32 v75, v18, v19
	v_pk_add_f32 v[8:9], v[176:177], v[24:25] neg_lo:[0,1] neg_hi:[0,1]
	v_pk_add_f32 v[10:11], v[178:179], v[26:27] neg_lo:[0,1] neg_hi:[0,1]
	v_pk_add_f32 v[12:13], v[202:203], v[28:29] neg_lo:[0,1] neg_hi:[0,1]
	v_pk_add_f32 v[14:15], v[204:205], v[30:31] neg_lo:[0,1] neg_hi:[0,1]
	v_pk_add_f32 v[16:17], v[206:207], v[32:33] neg_lo:[0,1] neg_hi:[0,1]
	v_pk_add_f32 v[18:19], v[208:209], v[34:35] neg_lo:[0,1] neg_hi:[0,1]
	v_cvt_pk_bf16_f32 v78, v4, v5
	v_cvt_pk_bf16_f32 v79, v6, v7
	ds_read2_b64 v[4:7], v98 offset1:2
	ds_read2_b64 v[20:23], v98 offset0:4 offset1:6
	ds_read2_b64 v[24:27], v98 offset0:8 offset1:10
	ds_read2_b64 v[28:31], v98 offset0:12 offset1:14
	ds_read2_b64 v[32:35], v98 offset0:16 offset1:18
	ds_read2_b64 v[82:85], v98 offset0:20 offset1:22
	ds_read2_b64 v[86:89], v98 offset0:24 offset1:26
	ds_read2_b64 v[90:93], v98 offset0:28 offset1:30
	v_cvt_pk_bf16_f32 v80, v8, v9
	v_cvt_pk_bf16_f32 v81, v10, v11
	v_cvt_pk_bf16_f32 v94, v12, v13
	v_cvt_pk_bf16_f32 v95, v14, v15
	v_cvt_pk_bf16_f32 v96, v16, v17
	v_cvt_pk_bf16_f32 v97, v18, v19
	s_waitcnt lgkmcnt(7)
	v_mfma_f32_32x32x16_bf16 v[4:19], v[4:7], v[52:55], 0
	s_waitcnt lgkmcnt(6)
	v_mfma_f32_32x32x16_bf16 v[4:19], v[20:23], v[56:59], v[4:19]
	s_waitcnt lgkmcnt(5)
	v_mfma_f32_32x32x16_bf16 v[4:19], v[24:27], v[36:39], v[4:19]
	s_waitcnt lgkmcnt(4)
	v_mfma_f32_32x32x16_bf16 v[4:19], v[28:31], v[40:43], v[4:19]
	s_waitcnt lgkmcnt(3)
	v_mfma_f32_32x32x16_bf16 v[4:19], v[32:35], v[44:47], v[4:19]
	s_waitcnt lgkmcnt(2)
	v_mfma_f32_32x32x16_bf16 v[4:19], v[82:85], v[48:51], v[4:19]
	s_waitcnt lgkmcnt(1)
	v_mfma_f32_32x32x16_bf16 v[4:19], v[86:89], v[60:63], v[4:19]
	s_waitcnt lgkmcnt(0)
	v_mfma_f32_32x32x16_bf16 v[4:19], v[90:93], v[64:67], v[4:19]
	v_add_u32_e32 v24, 0x2000, v98
	ds_read2_b64 v[20:23], v24 offset0:32 offset1:34
	ds_read2_b64 v[82:85], v24 offset0:36 offset1:38
	ds_read2_b64 v[86:89], v24 offset0:40 offset1:42
	ds_read2_b64 v[90:93], v24 offset0:44 offset1:46
	ds_read2_b64 v[98:101], v24 offset0:48 offset1:50
	ds_read2_b64 v[102:105], v24 offset0:52 offset1:54
	ds_read2_b64 v[106:109], v24 offset0:56 offset1:58
	ds_read2_b64 v[110:113], v24 offset0:60 offset1:62
	s_waitcnt lgkmcnt(7)
	v_mfma_f32_32x32x16_bf16 v[20:35], v[20:23], v[52:55], 0
	s_waitcnt lgkmcnt(6)
	v_mfma_f32_32x32x16_bf16 v[20:35], v[82:85], v[56:59], v[20:35]
	s_waitcnt lgkmcnt(5)
	v_mfma_f32_32x32x16_bf16 v[20:35], v[86:89], v[36:39], v[20:35]
	s_waitcnt lgkmcnt(4)
	v_mfma_f32_32x32x16_bf16 v[20:35], v[90:93], v[40:43], v[20:35]
	s_waitcnt lgkmcnt(3)
	v_mfma_f32_32x32x16_bf16 v[20:35], v[98:101], v[44:47], v[20:35]
	s_waitcnt lgkmcnt(2)
	v_mfma_f32_32x32x16_bf16 v[20:35], v[102:105], v[48:51], v[20:35]
	s_waitcnt lgkmcnt(1)
	v_mfma_f32_32x32x16_bf16 v[20:35], v[106:109], v[60:63], v[20:35]
	s_waitcnt lgkmcnt(0)
	v_mfma_f32_32x32x16_bf16 v[20:35], v[110:113], v[64:67], v[20:35]
	v_add3_u32 v52, s33, v149, v153
	v_add_u32_e32 v64, 0x1000, v52
	ds_read2_b64 v[36:39], v52 offset1:2
	ds_read2_b64 v[40:43], v52 offset0:4 offset1:6
	ds_read2_b64 v[44:47], v52 offset0:8 offset1:10
	ds_read2_b64 v[48:51], v52 offset0:12 offset1:14
	ds_read2_b64 v[52:55], v64 offset0:32 offset1:34
	ds_read2_b64 v[56:59], v64 offset0:36 offset1:38
	ds_read2_b64 v[60:63], v64 offset0:40 offset1:42
	ds_read2_b64 v[64:67], v64 offset0:44 offset1:46
	s_waitcnt lgkmcnt(7)
	v_mfma_f32_32x32x16_bf16 v[4:19], v[36:39], v[68:71], v[4:19]
	s_waitcnt lgkmcnt(3)
	v_mfma_f32_32x32x16_bf16 v[20:35], v[52:55], v[68:71], v[20:35]
	v_mfma_f32_32x32x16_bf16 v[4:19], v[40:43], v[72:75], v[4:19]
	s_waitcnt lgkmcnt(2)
	v_mfma_f32_32x32x16_bf16 v[20:35], v[56:59], v[72:75], v[20:35]
	v_mfma_f32_32x32x16_bf16 v[4:19], v[44:47], v[78:81], v[4:19]
	s_waitcnt lgkmcnt(1)
	v_mfma_f32_32x32x16_bf16 v[20:35], v[60:63], v[78:81], v[20:35]
	v_mfma_f32_32x32x16_bf16 v[4:19], v[48:51], v[94:97], v[4:19]
	s_waitcnt lgkmcnt(0)
	v_mfma_f32_32x32x16_bf16 v[20:35], v[64:67], v[94:97], v[20:35]
	v_lshl_add_u64 v[36:37], v[76:77], 0, v[2:3]
	s_mov_b32 s9, 0x479e0000
	v_add_co_u32_e32 v38, vcc, s9, v36
	s_mov_b32 s9, 0x479e1000
	s_nop 0
	v_addc_co_u32_e32 v39, vcc, 0, v37, vcc
	s_nop 3
	global_store_dword v[38:39], v4, off
	global_store_dword v[38:39], v5, off offset:2048
	v_add_co_u32_e32 v4, vcc, s9, v36
	s_mov_b32 s9, 0x479e4000
	s_nop 0
	v_addc_co_u32_e32 v5, vcc, 0, v37, vcc
	global_store_dword v[4:5], v6, off
	global_store_dword v[4:5], v7, off offset:2048
	v_add_co_u32_e32 v4, vcc, s9, v36
	s_mov_b32 s9, 0x479e5000
	s_nop 0
	v_addc_co_u32_e32 v5, vcc, 0, v37, vcc
	global_store_dword v[4:5], v8, off
	global_store_dword v[4:5], v9, off offset:2048
	v_add_co_u32_e32 v4, vcc, s9, v36
	s_mov_b32 s9, 0x479e8000
	s_nop 0
	v_addc_co_u32_e32 v5, vcc, 0, v37, vcc
	global_store_dword v[4:5], v10, off
	global_store_dword v[4:5], v11, off offset:2048
	v_add_co_u32_e32 v4, vcc, s9, v36
	s_mov_b32 s9, 0x479e9000
	s_nop 0
	v_addc_co_u32_e32 v5, vcc, 0, v37, vcc
	global_store_dword v[4:5], v12, off
	global_store_dword v[4:5], v13, off offset:2048
	v_add_co_u32_e32 v4, vcc, s9, v36
	s_mov_b32 s9, 0x479ec000
	s_nop 0
	v_addc_co_u32_e32 v5, vcc, 0, v37, vcc
	global_store_dword v[4:5], v14, off
	global_store_dword v[4:5], v15, off offset:2048
	v_add_co_u32_e32 v4, vcc, s9, v36
	s_mov_b32 s9, 0x479ed000
	s_nop 0
	v_addc_co_u32_e32 v5, vcc, 0, v37, vcc
	global_store_dword v[4:5], v16, off
	global_store_dword v[4:5], v17, off offset:2048
	v_add_co_u32_e32 v4, vcc, s9, v36
	s_mov_b32 s9, 0x479f0000
	s_nop 0
	v_addc_co_u32_e32 v5, vcc, 0, v37, vcc
	global_store_dword v[4:5], v18, off
	global_store_dword v[4:5], v19, off offset:2048
	v_add_co_u32_e32 v4, vcc, s9, v36
	s_mov_b32 s9, 0x479f1000
	s_nop 0
	v_addc_co_u32_e32 v5, vcc, 0, v37, vcc
	global_store_dword v[4:5], v20, off
	global_store_dword v[4:5], v21, off offset:2048
	v_add_co_u32_e32 v4, vcc, s9, v36
	s_mov_b32 s9, 0x479f4000
	s_nop 0
	v_addc_co_u32_e32 v5, vcc, 0, v37, vcc
	global_store_dword v[4:5], v22, off
	global_store_dword v[4:5], v23, off offset:2048
	v_add_co_u32_e32 v4, vcc, s9, v36
	s_mov_b32 s9, 0x479f5000
	s_nop 0
	v_addc_co_u32_e32 v5, vcc, 0, v37, vcc
	global_store_dword v[4:5], v24, off
	global_store_dword v[4:5], v25, off offset:2048
	v_add_co_u32_e32 v4, vcc, s9, v36
	s_mov_b32 s9, 0x479f8000
	s_nop 0
	v_addc_co_u32_e32 v5, vcc, 0, v37, vcc
	global_store_dword v[4:5], v26, off
	global_store_dword v[4:5], v27, off offset:2048
	v_add_co_u32_e32 v4, vcc, s9, v36
	s_mov_b32 s9, 0x479f9000
	s_nop 0
	v_addc_co_u32_e32 v5, vcc, 0, v37, vcc
	global_store_dword v[4:5], v28, off
	global_store_dword v[4:5], v29, off offset:2048
	v_add_co_u32_e32 v4, vcc, s9, v36
	s_mov_b32 s9, 0x479fc000
	s_nop 0
	v_addc_co_u32_e32 v5, vcc, 0, v37, vcc
	global_store_dword v[4:5], v30, off
	global_store_dword v[4:5], v31, off offset:2048
	v_add_co_u32_e32 v4, vcc, s9, v36
	s_nop 1
	v_addc_co_u32_e32 v5, vcc, 0, v37, vcc
	global_store_dword v[4:5], v32, off
	global_store_dword v[4:5], v33, off offset:2048
	v_add_co_u32_e32 v4, vcc, 0x479fd000, v36
	s_nop 1
	v_addc_co_u32_e32 v5, vcc, 0, v37, vcc
	global_store_dword v[4:5], v34, off
	global_store_dword v[4:5], v35, off offset:2048
	s_mov_b64 s[28:29], 0
	s_waitcnt lgkmcnt(0)
	s_barrier

.LBB0_497:
	v_add3_u32 v167, v2, v161, s59
	s_waitcnt vmcnt(14) lgkmcnt(0)
.Lscan_w1_join:
	ds_write2_b64 v167, v[4:5], v[6:7] offset1:1
	v_add_u32_e32 v167, v157, v161
	ds_write2_b64 v167, v[8:9], v[10:11] offset1:1
	v_add3_u32 v167, v2, v162, s59
	ds_write2_b64 v167, v[12:13], v[14:15] offset1:1
	v_add_u32_e32 v167, v157, v162
	ds_write2_b64 v167, v[16:17], v[18:19] offset1:1
	v_add3_u32 v167, v2, v163, s59
	ds_write2_b64 v167, v[20:21], v[22:23] offset1:1
	v_add_u32_e32 v167, v157, v163
	ds_write2_b64 v167, v[24:25], v[26:27] offset1:1
	v_add3_u32 v167, v2, v156, s59
	ds_write2_b64 v167, v[28:29], v[30:31] offset1:1
	v_add_u32_e32 v167, v157, v156
	ds_write2_b64 v167, v[32:33], v[34:35] offset1:1
	v_add_u32_e32 v167, v158, v164
	ds_write2_b64 v167, v[36:37], v[38:39] offset1:1
	v_add_u32_e32 v167, v158, v1
	ds_write2_b64 v167, v[40:41], v[42:43] offset1:1
	v_add_u32_e32 v167, v159, v164
	ds_write2_b64 v167, v[52:53], v[54:55] offset1:1
	v_add_u32_e32 v167, v159, v1
	ds_write2_b64 v167, v[56:57], v[58:59] offset1:1
	v_add_u32_e32 v167, v159, v165
	ds_write2_b64 v167, v[76:77], v[78:79] offset1:1
	v_add_u32_e32 v167, v159, v166
	s_cmp_gt_u32 s12, 60
	ds_write2_b64 v167, v[80:81], v[82:83] offset1:1
	s_waitcnt lgkmcnt(0)
	s_barrier
	s_cbranch_scc1 .LBB0_499
	v_add_co_u32_e32 v4, vcc, 0x43a30000, v154
	s_nop 1
	v_addc_co_u32_e32 v5, vcc, 0, v155, vcc
	v_add_co_u32_e32 v8, vcc, 0x44a30000, v154
	s_nop 1
	v_addc_co_u32_e32 v9, vcc, 0, v155, vcc
	v_add_co_u32_e32 v12, vcc, 0x43a30000, v152
	global_load_dwordx4 v[4:7], v[4:5], off
	s_nop 0
	global_load_dwordx4 v[8:11], v[8:9], off
	v_addc_co_u32_e32 v13, vcc, 0, v153, vcc
	v_add_co_u32_e32 v16, vcc, 0x44a30000, v152
	s_nop 1
	v_addc_co_u32_e32 v17, vcc, 0, v153, vcc
	v_add_co_u32_e32 v20, vcc, 0x43a30000, v150
	global_load_dwordx4 v[12:15], v[12:13], off
	s_nop 0
	global_load_dwordx4 v[16:19], v[16:17], off
	v_addc_co_u32_e32 v21, vcc, 0, v151, vcc
	v_add_co_u32_e32 v24, vcc, 0x44a30000, v150
	s_nop 1
	v_addc_co_u32_e32 v25, vcc, 0, v151, vcc
	v_add_co_u32_e32 v28, vcc, 0x43a30000, v148
	global_load_dwordx4 v[20:23], v[20:21], off
	s_nop 0
	global_load_dwordx4 v[24:27], v[24:25], off
	v_addc_co_u32_e32 v29, vcc, 0, v149, vcc
	v_add_co_u32_e32 v32, vcc, 0x44a30000, v148
	s_nop 1
	v_addc_co_u32_e32 v33, vcc, 0, v149, vcc
	v_add_co_u32_e32 v36, vcc, 0x46a06000, v146
	global_load_dwordx4 v[28:31], v[28:29], off
	s_nop 0
	global_load_dwordx4 v[32:35], v[32:33], off
	v_addc_co_u32_e32 v37, vcc, 0, v147, vcc
	v_add_co_u32_e32 v40, vcc, 0x46a06000, v144
	s_nop 1
	v_addc_co_u32_e32 v41, vcc, 0, v145, vcc
	v_add_co_u32_e32 v52, vcc, 0x45a0c000, v142
	global_load_dwordx4 v[36:39], v[36:37], off
	s_nop 0
	global_load_dwordx4 v[40:43], v[40:41], off
	v_addc_co_u32_e32 v53, vcc, 0, v143, vcc
	v_add_co_u32_e32 v56, vcc, 0x45a0c000, v140
	s_nop 1
	v_addc_co_u32_e32 v57, vcc, 0, v141, vcc
	v_add_co_u32_e32 v76, vcc, 0x45a0c000, v138
	global_load_dwordx4 v[52:55], v[52:53], off
	s_nop 0
	global_load_dwordx4 v[56:59], v[56:57], off
	v_addc_co_u32_e32 v77, vcc, 0, v139, vcc
	v_add_co_u32_e32 v80, vcc, 0x45a0c000, v136
	s_nop 1
	v_addc_co_u32_e32 v81, vcc, 0, v137, vcc
	global_load_dwordx4 v[76:79], v[76:77], off
	s_nop 0
	global_load_dwordx4 v[80:83], v[80:81], off
.LBB0_499:
	s_andn2_b64 vcc, exec, s[10:11]
	s_mov_b64 s[10:11], 0x20000
	s_cbranch_vccnz .LBB0_494
	s_waitcnt vmcnt(14)
	v_add_u32_e32 v136, v2, v161
	ds_write2_b64 v136, v[48:49], v[50:51] offset1:1
	v_add_u32_e32 v136, 0x4200, v136
	ds_write2_b64 v136, v[44:45], v[46:47] offset1:1
	v_add_u32_e32 v136, v2, v162
	ds_write2_b64 v136, v[64:65], v[66:67] offset1:1
	v_add_u32_e32 v136, 0x4200, v136
	ds_write2_b64 v136, v[60:61], v[62:63] offset1:1
	v_add_u32_e32 v136, v2, v163
	ds_write2_b64 v136, v[72:73], v[74:75] offset1:1
	v_add_u32_e32 v136, 0x4200, v136
	ds_write2_b64 v136, v[68:69], v[70:71] offset1:1
	v_add_u32_e32 v136, v2, v156
	ds_write2_b64 v136, v[88:89], v[90:91] offset1:1
	v_add_u32_e32 v136, 0x4200, v136
	ds_write2_b64 v136, v[84:85], v[86:87] offset1:1
	v_add_u32_e32 v136, v160, v164
	v_add_u32_e32 v137, 0x8400, v136
	ds_write2_b64 v137, v[92:93], v[94:95] offset1:1
	v_add_u32_e32 v137, v160, v1
	v_add_u32_e32 v138, 0x8400, v137
	v_add_u32_e32 v136, 0xa600, v136
	ds_write2_b64 v138, v[96:97], v[98:99] offset1:1
	ds_write2_b64 v136, v[100:101], v[102:103] offset1:1
	v_add_u32_e32 v136, 0xa600, v137
	ds_write2_b64 v136, v[104:105], v[106:107] offset1:1
	v_add3_u32 v136, v160, v165, s58
	ds_write2_b64 v136, v[108:109], v[110:111] offset1:1
	v_add3_u32 v136, v160, v166, s58
	ds_write2_b64 v136, v[112:113], v[114:115] offset1:1
	s_branch .LBB0_494
.Lscan_w1_full:
	v_add3_u32 v167, v2, v161, s59
	s_waitcnt vmcnt(0) lgkmcnt(0)
	s_branch .Lscan_w1_join

.LBB0_506:
	s_or_b64 exec, exec, s[8:9]
	v_mov_b32_e32 v1, s12
	s_waitcnt lgkmcnt(0)
	s_barrier
	ds_read_b32 v1, v1
	s_movk_i32 s8, 0x1ff
	s_waitcnt lgkmcnt(0)
	v_cmp_lt_i32_e32 vcc, s8, v1
	v_readfirstlane_b32 s16, v1
	s_mov_b64 s[8:9], -1
	s_cbranch_vccnz .LBB0_503
	v_mov_b32_e32 v1, v0
	s_lshl_b32 s15, s16, 3
	v_readlane_b32 s8, v252, 0
	v_readfirstlane_b32 s17, v1
	s_mov_b32 s9, s88
	s_andn2_b32 s15, s15, 31
	s_ashr_i32 s14, s17, 6
	s_mov_b64 s[10:11], s[68:69]
	s_add_u32 s8, s10, 0x9000000
	s_addc_u32 s9, s11, 0
	s_lshl_b32 s16, s16, 12
	s_and_b32 s18, s16, 0x3000
	s_sub_i32 s16, s18, s15
	s_addk_i32 s16, 0xfe0
	s_waitcnt vmcnt(0)
	v_ashrrev_i32_e32 v9, 7, v1
	v_lshlrev_b32_e32 v2, 4, v1
	v_add_u32_e32 v4, s16, v9
	v_mov_b64_e32 v[10:11], s[10:11]
	s_movk_i32 s19, 0xc00
	v_and_b32_e32 v2, 0x7f0, v2
	v_mad_i64_i32 v[4:5], s[20:21], v4, s19, v[10:11]
	v_lshl_add_u64 v[4:5], v[4:5], 0, v[2:3]
	s_mov_b32 s22, 0x2de00000
	v_add_co_u32_e32 v4, vcc, s22, v4
	s_nop 1
	v_addc_co_u32_e32 v5, vcc, 0, v5, vcc
	s_barrier
	global_load_dwordx4 v[4:7], v[4:5], off offset:1024
	v_add_u32_e32 v8, s72, v2
	s_movk_i32 s23, 0x810
	v_mad_u64_u32 v[12:13], s[20:21], v9, s23, v[8:9]
	s_sub_i32 s15, 0x1020, s15
	s_lshr_b32 s15, s15, 6
	s_cmp_ge_i32 s14, s15
	s_waitcnt vmcnt(0) lgkmcnt(0)
	ds_write_b128 v12, v[4:7]
	v_add_u32_e32 v4, 0x200, v1
	v_ashrrev_i32_e32 v9, 7, v4
	v_add_u32_e32 v4, s16, v9
	v_mad_i64_i32 v[4:5], s[20:21], v4, s19, v[10:11]
	v_lshl_add_u64 v[4:5], v[4:5], 0, v[2:3]
	v_add_co_u32_e32 v4, vcc, s22, v4
	v_mad_u64_u32 v[12:13], s[20:21], v9, s23, v[8:9]
	s_nop 0
	v_addc_co_u32_e32 v5, vcc, 0, v5, vcc
	global_load_dwordx4 v[4:7], v[4:5], off offset:1024
	s_waitcnt vmcnt(0) lgkmcnt(0)
	ds_write_b128 v12, v[4:7]
	v_add_u32_e32 v4, 0x400, v1
	v_ashrrev_i32_e32 v9, 7, v4
	v_add_u32_e32 v4, s16, v9
	v_mad_i64_i32 v[4:5], s[20:21], v4, s19, v[10:11]
	v_lshl_add_u64 v[4:5], v[4:5], 0, v[2:3]
	v_add_co_u32_e32 v4, vcc, s22, v4
	v_mad_u64_u32 v[12:13], s[20:21], v9, s23, v[8:9]
	s_nop 0
	v_addc_co_u32_e32 v5, vcc, 0, v5, vcc
	global_load_dwordx4 v[4:7], v[4:5], off offset:1024
	s_waitcnt vmcnt(0) lgkmcnt(0)
	ds_write_b128 v12, v[4:7]
	v_add_u32_e32 v4, 0x600, v1
	v_ashrrev_i32_e32 v9, 7, v4
	v_add_u32_e32 v4, s16, v9
	v_mad_i64_i32 v[4:5], s[20:21], v4, s19, v[10:11]
	v_lshl_add_u64 v[4:5], v[4:5], 0, v[2:3]
	v_add_co_u32_e32 v4, vcc, s22, v4
	v_mad_u64_u32 v[12:13], s[20:21], v9, s23, v[8:9]
	s_nop 0
	v_addc_co_u32_e32 v5, vcc, 0, v5, vcc
	global_load_dwordx4 v[4:7], v[4:5], off offset:1024
	s_waitcnt vmcnt(0) lgkmcnt(0)
	ds_write_b128 v12, v[4:7]
	v_add_u32_e32 v4, 0x800, v1
	v_ashrrev_i32_e32 v9, 7, v4
	v_add_u32_e32 v4, s16, v9
	v_mad_i64_i32 v[4:5], s[20:21], v4, s19, v[10:11]
	v_lshl_add_u64 v[4:5], v[4:5], 0, v[2:3]
	v_add_co_u32_e32 v4, vcc, s22, v4
	v_mad_u64_u32 v[12:13], s[20:21], v9, s23, v[8:9]
	s_nop 0
	v_addc_co_u32_e32 v5, vcc, 0, v5, vcc
	global_load_dwordx4 v[4:7], v[4:5], off offset:1024
	s_waitcnt vmcnt(0) lgkmcnt(0)
	ds_write_b128 v12, v[4:7]
	v_add_u32_e32 v4, 0xa00, v1
	v_ashrrev_i32_e32 v9, 7, v4
	v_add_u32_e32 v4, s16, v9
	v_mad_i64_i32 v[4:5], s[20:21], v4, s19, v[10:11]
	v_lshl_add_u64 v[4:5], v[4:5], 0, v[2:3]
	v_add_co_u32_e32 v4, vcc, s22, v4
	v_mad_u64_u32 v[12:13], s[20:21], v9, s23, v[8:9]
	s_nop 0
	v_addc_co_u32_e32 v5, vcc, 0, v5, vcc
	global_load_dwordx4 v[4:7], v[4:5], off offset:1024
	s_waitcnt vmcnt(0) lgkmcnt(0)
	ds_write_b128 v12, v[4:7]
	v_add_u32_e32 v4, 0xc00, v1
	v_ashrrev_i32_e32 v9, 7, v4
	v_add_u32_e32 v4, s16, v9
	v_mad_i64_i32 v[4:5], s[20:21], v4, s19, v[10:11]
	v_lshl_add_u64 v[4:5], v[4:5], 0, v[2:3]
	v_add_co_u32_e32 v4, vcc, s22, v4
	v_mad_u64_u32 v[12:13], s[20:21], v9, s23, v[8:9]
	s_nop 0
	v_addc_co_u32_e32 v5, vcc, 0, v5, vcc
	global_load_dwordx4 v[4:7], v[4:5], off offset:1024
	s_waitcnt vmcnt(0) lgkmcnt(0)
	ds_write_b128 v12, v[4:7]
	v_add_u32_e32 v4, 0xe00, v1
	v_ashrrev_i32_e32 v9, 7, v4
	v_add_u32_e32 v4, s16, v9
	v_mad_i64_i32 v[4:5], s[20:21], v4, s19, v[10:11]
	v_lshl_add_u64 v[4:5], v[4:5], 0, v[2:3]
	v_add_co_u32_e32 v4, vcc, s22, v4
	v_mad_u64_u32 v[8:9], s[20:21], v9, s23, v[8:9]
	s_nop 0
	v_addc_co_u32_e32 v5, vcc, 0, v5, vcc
	global_load_dwordx4 v[4:7], v[4:5], off offset:1024
	s_movk_i32 s19, 0x3000
	s_waitcnt vmcnt(0) lgkmcnt(0)
	ds_write_b128 v8, v[4:7]
	v_ashrrev_i32_e32 v6, 4, v1
	v_and_b32_e32 v7, 15, v1
	v_add_u32_e32 v2, s16, v6
	v_mov_b64_e32 v[4:5], s[8:9]
	v_mad_i64_i32 v[4:5], s[20:21], v2, s24, v[4:5]
	v_lshlrev_b32_e32 v2, 1, v7
	v_lshl_add_u64 v[4:5], v[4:5], 0, v[2:3]
	v_add_co_u32_e32 v4, vcc, s19, v4
	s_mov_b64 s[20:21], 0x3100
	s_nop 0
	v_addc_co_u32_e32 v5, vcc, 0, v5, vcc
	global_load_ushort v2, v[4:5], off offset:384
	v_lshlrev_b32_e32 v4, 7, v7
	v_lshlrev_b32_e32 v5, 2, v6
	v_add3_u32 v4, s13, v4, v5
	s_waitcnt vmcnt(0) lgkmcnt(0)
	v_lshlrev_b32_e32 v2, 16, v2
	v_mul_f32_e32 v2, 0x3d000000, v2
	ds_write_b32 v4, v2
	s_waitcnt lgkmcnt(0)
	s_barrier
	s_cbranch_scc1 .LBB0_502
	s_andn2_b32 s17, s17, 63
	v_and_b32_e32 v5, 31, v1
	s_add_i32 s17, s17, s18
	v_or_b32_e32 v12, s17, v5
	v_bfe_u32 v2, v1, 5, 1
	v_or_b32_e32 v8, 32, v12
	v_mov_b64_e32 v[6:7], s[8:9]
	v_lshlrev_b32_e32 v4, 3, v2
	v_or_b32_e32 v1, s18, v5
	v_mad_i64_i32 v[8:9], s[18:19], v8, s24, v[6:7]
	v_lshlrev_b32_e32 v2, 4, v2
	v_lshl_add_u64 v[8:9], v[8:9], 0, v[2:3]
	s_movk_i32 s17, 0x3000
	v_lshl_add_u64 v[10:11], v[8:9], 0, s[20:21]
	v_add_co_u32_e32 v8, vcc, s17, v8
	v_mad_i64_i32 v[6:7], s[18:19], v12, s24, v[6:7]
	s_nop 0
	v_addc_co_u32_e32 v9, vcc, 0, v9, vcc
	v_lshl_add_u64 v[6:7], v[6:7], 0, v[2:3]
	global_load_dwordx4 v[36:39], v[10:11], off offset:96
	global_load_dwordx4 v[44:47], v[10:11], off offset:64
	global_load_dwordx4 v[40:43], v[10:11], off offset:32
	global_load_dwordx4 v[48:51], v[8:9], off offset:256
	v_lshl_add_u64 v[8:9], v[6:7], 0, s[20:21]
	v_add_co_u32_e32 v6, vcc, s17, v6
	global_load_dwordx4 v[52:55], v[8:9], off offset:96
	global_load_dwordx4 v[60:63], v[8:9], off offset:64
	global_load_dwordx4 v[56:59], v[8:9], off offset:32
	v_addc_co_u32_e32 v7, vcc, 0, v7, vcc
	global_load_dwordx4 v[64:67], v[6:7], off offset:256
	v_mul_u32_u24_e32 v6, 0x810, v5
	v_lshl_add_u32 v134, v5, 2, s13
	v_add3_u32 v135, s72, v6, v2
	v_or_b32_e32 v5, s16, v5
	v_mov_b64_e32 v[6:7], s[10:11]
	s_movk_i32 s10, 0x4100
	v_mad_u64_u32 v[6:7], s[10:11], v5, s10, v[6:7]
	v_lshl_add_u64 v[6:7], v[6:7], 0, v[2:3]
	s_mov_b64 s[10:11], 0x30e00000
	v_lshl_add_u64 v[132:133], v[6:7], 0, s[10:11]
	v_lshlrev_b32_e32 v2, 1, v4
	s_waitcnt vmcnt(0)

.LBB0_510:
	ds_read_b32 v216, v134
	ds_read_b128 v[146:149], v135
	ds_read_b128 v[150:153], v135 offset:32
	ds_read_b128 v[154:157], v135 offset:64
	ds_read_b128 v[158:161], v135 offset:96
	v_mov_b32_e32 v217, 0
	v_mov_b32_e32 v178, 0
	v_mov_b32_e32 v179, 0
	v_mov_b32_e32 v180, 0
	v_mov_b32_e32 v181, 0
	v_mov_b32_e32 v182, 0
	v_mov_b32_e32 v183, 0
	v_mov_b32_e32 v184, 0
	v_mov_b32_e32 v185, 0
	v_mov_b32_e32 v186, 0
	v_mov_b32_e32 v187, 0
	v_mov_b32_e32 v188, 0
	v_mov_b32_e32 v189, 0
	v_mov_b32_e32 v190, 0
	v_mov_b32_e32 v191, 0
	v_mov_b32_e32 v192, 0
	v_mov_b32_e32 v193, 0
	v_mov_b32_e32 v196, 0
	v_mov_b32_e32 v197, 0
	v_mov_b32_e32 v198, 0
	v_mov_b32_e32 v199, 0
	v_mov_b32_e32 v200, 0
	v_mov_b32_e32 v201, 0
	v_mov_b32_e32 v202, 0
	v_mov_b32_e32 v203, 0
	v_mov_b32_e32 v204, 0
	v_mov_b32_e32 v205, 0
	v_mov_b32_e32 v206, 0
	v_mov_b32_e32 v207, 0
	v_mov_b32_e32 v208, 0
	v_mov_b32_e32 v209, 0
	v_mov_b32_e32 v210, 0
	v_mov_b32_e32 v211, 0
.Lidx_head_loop:
	v_add_u32_e32 v219, s17, v134
	v_add_u32_e32 v220, s17, v135
	v_mov_b32_e32 v218, v217
	ds_read_b32 v217, v219 offset:128
	ds_read_b128 v[162:165], v220 offset:128
	ds_read_b128 v[166:169], v220 offset:160
	ds_read_b128 v[170:173], v220 offset:192
	ds_read_b128 v[174:177], v220 offset:224
	s_waitcnt lgkmcnt(5)
	v_mfma_f32_32x32x16_bf16 v[4:19], v[48:51], v[146:149], 0
	v_max_i32_e32 v178, 0, v178
	v_max_i32_e32 v179, 0, v179
	v_max_i32_e32 v180, 0, v180
	v_max_i32_e32 v181, 0, v181
	v_fmac_f32_e32 v116, v218, v178
	v_fmac_f32_e32 v117, v218, v179
	v_fmac_f32_e32 v118, v218, v180
	v_fmac_f32_e32 v119, v218, v181
	v_mfma_f32_32x32x16_bf16 v[20:35], v[64:67], v[146:149], 0
	v_max_i32_e32 v182, 0, v182
	v_max_i32_e32 v183, 0, v183
	v_max_i32_e32 v184, 0, v184
	v_max_i32_e32 v185, 0, v185
	v_fmac_f32_e32 v112, v218, v182
	v_fmac_f32_e32 v113, v218, v183
	v_fmac_f32_e32 v114, v218, v184
	v_fmac_f32_e32 v115, v218, v185
	v_mfma_f32_32x32x16_bf16 v[4:19], v[40:43], v[150:153], v[4:19]
	v_max_i32_e32 v186, 0, v186
	v_max_i32_e32 v187, 0, v187
	v_max_i32_e32 v188, 0, v188
	v_max_i32_e32 v189, 0, v189
	v_fmac_f32_e32 v104, v218, v186
	v_fmac_f32_e32 v105, v218, v187
	v_fmac_f32_e32 v106, v218, v188
	v_fmac_f32_e32 v107, v218, v189
	v_mfma_f32_32x32x16_bf16 v[20:35], v[56:59], v[150:153], v[20:35]
	v_max_i32_e32 v190, 0, v190
	v_max_i32_e32 v191, 0, v191
	v_max_i32_e32 v192, 0, v192
	v_max_i32_e32 v193, 0, v193
	v_fmac_f32_e32 v100, v218, v190
	v_fmac_f32_e32 v101, v218, v191
	v_fmac_f32_e32 v102, v218, v192
	v_fmac_f32_e32 v103, v218, v193
	v_mfma_f32_32x32x16_bf16 v[4:19], v[44:47], v[154:157], v[4:19]
	v_max_i32_e32 v196, 0, v196
	v_max_i32_e32 v197, 0, v197
	v_max_i32_e32 v198, 0, v198
	v_max_i32_e32 v199, 0, v199
	v_fmac_f32_e32 v128, v218, v196
	v_fmac_f32_e32 v129, v218, v197
	v_fmac_f32_e32 v130, v218, v198
	v_fmac_f32_e32 v131, v218, v199
	v_mfma_f32_32x32x16_bf16 v[20:35], v[60:63], v[154:157], v[20:35]
	v_max_i32_e32 v200, 0, v200
	v_max_i32_e32 v201, 0, v201
	v_max_i32_e32 v202, 0, v202
	v_max_i32_e32 v203, 0, v203
	v_fmac_f32_e32 v124, v218, v200
	v_fmac_f32_e32 v125, v218, v201
	v_fmac_f32_e32 v126, v218, v202
	v_fmac_f32_e32 v127, v218, v203
	v_mfma_f32_32x32x16_bf16 v[4:19], v[36:39], v[158:161], v[4:19]
	v_max_i32_e32 v204, 0, v204
	v_max_i32_e32 v205, 0, v205
	v_max_i32_e32 v206, 0, v206
	v_max_i32_e32 v207, 0, v207
	v_fmac_f32_e32 v120, v218, v204
	v_fmac_f32_e32 v121, v218, v205
	v_fmac_f32_e32 v122, v218, v206
	v_fmac_f32_e32 v123, v218, v207
	v_mfma_f32_32x32x16_bf16 v[20:35], v[52:55], v[158:161], v[20:35]
	v_max_i32_e32 v208, 0, v208
	v_max_i32_e32 v209, 0, v209
	v_max_i32_e32 v210, 0, v210
	v_max_i32_e32 v211, 0, v211
	v_fmac_f32_e32 v108, v218, v208
	v_fmac_f32_e32 v109, v218, v209
	v_fmac_f32_e32 v110, v218, v210
	v_fmac_f32_e32 v111, v218, v211
	v_mov_b32_e32 v218, v216
	ds_read_b32 v216, v219 offset:256
	ds_read_b128 v[146:149], v220 offset:256
	ds_read_b128 v[150:153], v220 offset:288
	ds_read_b128 v[154:157], v220 offset:320
	ds_read_b128 v[158:161], v220 offset:352
	s_waitcnt lgkmcnt(5)
	v_mfma_f32_32x32x16_bf16 v[178:193], v[48:51], v[162:165], 0
	v_max_i32_e32 v4, 0, v4
	v_max_i32_e32 v5, 0, v5
	v_max_i32_e32 v6, 0, v6
	v_max_i32_e32 v7, 0, v7
	v_fmac_f32_e32 v116, v218, v4
	v_fmac_f32_e32 v117, v218, v5
	v_fmac_f32_e32 v118, v218, v6
	v_fmac_f32_e32 v119, v218, v7
	v_mfma_f32_32x32x16_bf16 v[196:211], v[64:67], v[162:165], 0
	v_max_i32_e32 v8, 0, v8
	v_max_i32_e32 v9, 0, v9
	v_max_i32_e32 v10, 0, v10
	v_max_i32_e32 v11, 0, v11
	v_fmac_f32_e32 v112, v218, v8
	v_fmac_f32_e32 v113, v218, v9
	v_fmac_f32_e32 v114, v218, v10
	v_fmac_f32_e32 v115, v218, v11
	v_mfma_f32_32x32x16_bf16 v[178:193], v[40:43], v[166:169], v[178:193]
	v_max_i32_e32 v12, 0, v12
	v_max_i32_e32 v13, 0, v13
	v_max_i32_e32 v14, 0, v14
	v_max_i32_e32 v15, 0, v15
	v_fmac_f32_e32 v104, v218, v12
	v_fmac_f32_e32 v105, v218, v13
	v_fmac_f32_e32 v106, v218, v14
	v_fmac_f32_e32 v107, v218, v15
	v_mfma_f32_32x32x16_bf16 v[196:211], v[56:59], v[166:169], v[196:211]
	v_max_i32_e32 v16, 0, v16
	v_max_i32_e32 v17, 0, v17
	v_max_i32_e32 v18, 0, v18
	v_max_i32_e32 v19, 0, v19
	v_fmac_f32_e32 v100, v218, v16
	v_fmac_f32_e32 v101, v218, v17
	v_fmac_f32_e32 v102, v218, v18
	v_fmac_f32_e32 v103, v218, v19
	v_mfma_f32_32x32x16_bf16 v[178:193], v[44:47], v[170:173], v[178:193]
	v_max_i32_e32 v20, 0, v20
	v_max_i32_e32 v21, 0, v21
	v_max_i32_e32 v22, 0, v22
	v_max_i32_e32 v23, 0, v23
	v_fmac_f32_e32 v128, v218, v20
	v_fmac_f32_e32 v129, v218, v21
	v_fmac_f32_e32 v130, v218, v22
	v_fmac_f32_e32 v131, v218, v23
	v_mfma_f32_32x32x16_bf16 v[196:211], v[60:63], v[170:173], v[196:211]
	v_max_i32_e32 v24, 0, v24
	v_max_i32_e32 v25, 0, v25
	v_max_i32_e32 v26, 0, v26
	v_max_i32_e32 v27, 0, v27
	v_fmac_f32_e32 v124, v218, v24
	v_fmac_f32_e32 v125, v218, v25
	v_fmac_f32_e32 v126, v218, v26
	v_fmac_f32_e32 v127, v218, v27
	v_mfma_f32_32x32x16_bf16 v[178:193], v[36:39], v[174:177], v[178:193]
	v_max_i32_e32 v28, 0, v28
	v_max_i32_e32 v29, 0, v29
	v_max_i32_e32 v30, 0, v30
	v_max_i32_e32 v31, 0, v31
	v_fmac_f32_e32 v120, v218, v28
	v_fmac_f32_e32 v121, v218, v29
	v_fmac_f32_e32 v122, v218, v30
	v_fmac_f32_e32 v123, v218, v31
	v_mfma_f32_32x32x16_bf16 v[196:211], v[52:55], v[174:177], v[196:211]
	v_max_i32_e32 v32, 0, v32
	v_max_i32_e32 v33, 0, v33
	v_max_i32_e32 v34, 0, v34
	v_max_i32_e32 v35, 0, v35
	v_fmac_f32_e32 v108, v218, v32
	v_fmac_f32_e32 v109, v218, v33
	v_fmac_f32_e32 v110, v218, v34
	v_fmac_f32_e32 v111, v218, v35
	s_addk_i32 s17, 0x100
	s_cmpk_lg_i32 s17, 0x800
	s_cbranch_scc1 .Lidx_head_loop
	s_waitcnt lgkmcnt(0)
	s_nop 4
	v_max_i32_e32 v178, 0, v178
	v_max_i32_e32 v179, 0, v179
	v_max_i32_e32 v180, 0, v180
	v_max_i32_e32 v181, 0, v181
	v_fmac_f32_e32 v116, v217, v178
	v_fmac_f32_e32 v117, v217, v179
	v_fmac_f32_e32 v118, v217, v180
	v_fmac_f32_e32 v119, v217, v181
	v_max_i32_e32 v182, 0, v182
	v_max_i32_e32 v183, 0, v183
	v_max_i32_e32 v184, 0, v184
	v_max_i32_e32 v185, 0, v185
	v_fmac_f32_e32 v112, v217, v182
	v_fmac_f32_e32 v113, v217, v183
	v_fmac_f32_e32 v114, v217, v184
	v_fmac_f32_e32 v115, v217, v185
	v_max_i32_e32 v186, 0, v186
	v_max_i32_e32 v187, 0, v187
	v_max_i32_e32 v188, 0, v188
	v_max_i32_e32 v189, 0, v189
	v_fmac_f32_e32 v104, v217, v186
	v_fmac_f32_e32 v105, v217, v187
	v_fmac_f32_e32 v106, v217, v188
	v_fmac_f32_e32 v107, v217, v189
	v_max_i32_e32 v190, 0, v190
	v_max_i32_e32 v191, 0, v191
	v_max_i32_e32 v192, 0, v192
	v_max_i32_e32 v193, 0, v193
	v_fmac_f32_e32 v100, v217, v190
	v_fmac_f32_e32 v101, v217, v191
	v_fmac_f32_e32 v102, v217, v192
	v_fmac_f32_e32 v103, v217, v193
	v_max_i32_e32 v196, 0, v196
	v_max_i32_e32 v197, 0, v197
	v_max_i32_e32 v198, 0, v198
	v_max_i32_e32 v199, 0, v199
	v_fmac_f32_e32 v128, v217, v196
	v_fmac_f32_e32 v129, v217, v197
	v_fmac_f32_e32 v130, v217, v198
	v_fmac_f32_e32 v131, v217, v199
	v_max_i32_e32 v200, 0, v200
	v_max_i32_e32 v201, 0, v201
	v_max_i32_e32 v202, 0, v202
	v_max_i32_e32 v203, 0, v203
	v_fmac_f32_e32 v124, v217, v200
	v_fmac_f32_e32 v125, v217, v201
	v_fmac_f32_e32 v126, v217, v202
	v_fmac_f32_e32 v127, v217, v203
	v_max_i32_e32 v204, 0, v204
	v_max_i32_e32 v205, 0, v205
	v_max_i32_e32 v206, 0, v206
	v_max_i32_e32 v207, 0, v207
	v_fmac_f32_e32 v120, v217, v204
	v_fmac_f32_e32 v121, v217, v205
	v_fmac_f32_e32 v122, v217, v206
	v_fmac_f32_e32 v123, v217, v207
	v_max_i32_e32 v208, 0, v208
	v_max_i32_e32 v209, 0, v209
	v_max_i32_e32 v210, 0, v210
	v_max_i32_e32 v211, 0, v211
	v_fmac_f32_e32 v108, v217, v208
	v_fmac_f32_e32 v109, v217, v209
	v_fmac_f32_e32 v110, v217, v210
	v_fmac_f32_e32 v111, v217, v211
	s_waitcnt vmcnt(0)
	s_lshl_b32 s18, s14, 6
	s_ashr_i32 s19, s18, 31
	v_mov_b64_e32 v[64:65], v[80:81]
	v_mov_b64_e32 v[56:57], v[68:69]
	v_mov_b64_e32 v[60:61], v[72:73]
	v_mov_b64_e32 v[52:53], v[76:77]
	v_mov_b64_e32 v[48:49], v[96:97]
	v_mov_b64_e32 v[40:41], v[84:85]
	v_mov_b64_e32 v[44:45], v[88:89]
	v_mov_b64_e32 v[36:37], v[92:93]
	v_lshl_add_u64 v[4:5], s[18:19], 2, v[132:133]
	s_and_b64 vcc, exec, s[10:11]
	v_mov_b64_e32 v[66:67], v[82:83]
	v_mov_b64_e32 v[58:59], v[70:71]
	v_mov_b64_e32 v[62:63], v[74:75]
	v_mov_b64_e32 v[54:55], v[78:79]
	v_mov_b64_e32 v[50:51], v[98:99]
	v_mov_b64_e32 v[42:43], v[86:87]
	v_mov_b64_e32 v[46:47], v[90:91]
	v_mov_b64_e32 v[38:39], v[94:95]
	s_mov_b32 s14, s16
	global_store_dwordx4 v[4:5], v[128:131], off
	global_store_dwordx4 v[4:5], v[116:119], off offset:128
	global_store_dwordx4 v[4:5], v[124:127], off offset:32
	global_store_dwordx4 v[4:5], v[112:115], off offset:160
	global_store_dwordx4 v[4:5], v[120:123], off offset:64
	global_store_dwordx4 v[4:5], v[104:107], off offset:192
	global_store_dwordx4 v[4:5], v[108:111], off offset:96
	global_store_dwordx4 v[4:5], v[100:103], off offset:224
	s_cbranch_vccz .LBB0_509
	s_branch .LBB0_502

.LBB0_603:
	s_lshl_b64 s[0:1], s[4:5], 9
	v_readlane_b32 s2, v253, 60
	s_add_u32 s0, s2, s0
	v_readlane_b32 s2, v253, 61
	s_addc_u32 s1, s2, s1
	v_lshl_add_u64 v[6:7], v[74:75], 3, s[0:1]
	v_readlane_b32 s0, v253, 57
	s_xor_b32 s100, s4, 0x7ff
	s_bitcmp1_b32 s4, 11
	s_cselect_b32 s4, s100, s4
	s_add_i32 s4, s4, s0
	v_readlane_b32 s72, v254, 2
	s_cmpk_lt_i32 s4, 0x4000
	global_store_dwordx2 v[6:7], v[4:5], off
	s_cbranch_scc0 .LBB0_1152
.LBB0_604:
	s_xor_b32 s100, s4, 0x7ff
	s_bitcmp1_b32 s4, 11
	s_cselect_b32 s4, s100, s4
	s_mov_b32 s2, s4
	v_writelane_b32 v254, s2, 3
	s_and_b32 s33, s4, 0xfff
	s_mul_i32 s1, s4, 0x4100
	v_writelane_b32 v254, s3, 4
	v_readlane_b32 s2, v253, 58
	s_mul_hi_i32 s0, s4, 0x4100
	s_add_u32 s4, s2, s1
	v_readlane_b32 s1, v253, 59
	s_addc_u32 s5, s1, s0
	s_cmpk_lt_u32 s33, 0x200
	s_cselect_b64 s[0:1], -1, 0
	v_mov_b32_e32 v74, v76
	s_mov_b64 s[2:3], -1
	s_and_b64 vcc, exec, s[0:1]
	s_cbranch_vccz .LBB0_606
	v_min_i32_e32 v4, s33, v74
	s_waitcnt lgkmcnt(0)
	v_ashrrev_i32_e32 v5, 31, v4
	v_lshl_add_u64 v[4:5], v[4:5], 2, s[4:5]
	v_add_u32_e32 v11, 64, v74
	global_load_dword v1, v[4:5], off
	v_min_i32_e32 v4, s33, v11
	v_ashrrev_i32_e32 v5, 31, v4
	v_add_u32_e32 v10, 0x80, v74
	v_lshl_add_u64 v[4:5], v[4:5], 2, s[4:5]
	global_load_dword v12, v[4:5], off
	v_min_i32_e32 v4, s33, v10
	v_ashrrev_i32_e32 v5, 31, v4
	v_add_u32_e32 v9, 0xc0, v74
	v_lshl_add_u64 v[4:5], v[4:5], 2, s[4:5]
	global_load_dword v13, v[4:5], off
	v_min_i32_e32 v4, s33, v9
	v_ashrrev_i32_e32 v5, 31, v4
	v_add_u32_e32 v8, 0x100, v74
	v_lshl_add_u64 v[4:5], v[4:5], 2, s[4:5]
	global_load_dword v14, v[4:5], off
	v_min_i32_e32 v4, s33, v8
	v_ashrrev_i32_e32 v5, 31, v4
	v_add_u32_e32 v7, 0x140, v74
	v_lshl_add_u64 v[4:5], v[4:5], 2, s[4:5]
	global_load_dword v15, v[4:5], off
	v_min_i32_e32 v4, s33, v7
	v_ashrrev_i32_e32 v5, 31, v4
	v_add_u32_e32 v6, 0x180, v74
	v_lshl_add_u64 v[4:5], v[4:5], 2, s[4:5]
	global_load_dword v16, v[4:5], off
	v_min_i32_e32 v4, s33, v6
	v_ashrrev_i32_e32 v5, 31, v4
	v_add_u32_e32 v2, 0x1c0, v74
	v_lshl_add_u64 v[4:5], v[4:5], 2, s[4:5]
	global_load_dword v17, v[4:5], off
	v_min_i32_e32 v4, s33, v2
	v_ashrrev_i32_e32 v5, 31, v4
	v_lshl_add_u64 v[4:5], v[4:5], 2, s[4:5]
	global_load_dword v4, v[4:5], off
	v_cmp_ge_i32_e32 vcc, s33, v74
	s_mov_b64 s[2:3], 0
	s_waitcnt vmcnt(0) lgkmcnt(0)
	v_cndmask_b32_e32 v18, v229, v1, vcc
	v_cmp_ge_i32_e32 vcc, s33, v2
	s_nop 1
	v_cndmask_b32_e32 v25, v229, v4, vcc
	v_cmp_ge_i32_e32 vcc, s33, v6
	s_nop 1
	v_cndmask_b32_e32 v24, v229, v17, vcc
	v_cmp_ge_i32_e32 vcc, s33, v7
	s_nop 1
	v_cndmask_b32_e32 v23, v229, v16, vcc
	v_cmp_ge_i32_e32 vcc, s33, v8
	s_nop 1
	v_cndmask_b32_e32 v22, v229, v15, vcc
	v_cmp_ge_i32_e32 vcc, s33, v9
	s_nop 1
	v_cndmask_b32_e32 v21, v229, v14, vcc
	v_cmp_ge_i32_e32 vcc, s33, v10
	s_nop 1
	v_cndmask_b32_e32 v20, v229, v13, vcc
	v_cmp_ge_i32_e32 vcc, s33, v11
	s_nop 1
	v_cndmask_b32_e32 v19, v229, v12, vcc

.Lmix2_to_ret:
	v_writelane_b32 v255, s2, 1
	v_writelane_b32 v255, s3, 2
	v_writelane_b32 v255, s4, 3
	v_writelane_b32 v255, s5, 4
	s_branch .LBB0_1133
.Lmix2_after_ret:
	v_readlane_b32 s2, v255, 1
	v_readlane_b32 s3, v255, 2
	v_readlane_b32 s4, v255, 3
	v_readlane_b32 s5, v255, 4
	s_nop 3
	s_branch .LBB0_1325
